# cvt_f16 hand-written: fully contiguous 1 KB loads per wave instruction, lane-pair DPP exchange so stores stay 16 B and contiguous
# speedup vs baseline: 1.1908x; 1.0246x over previous
_Z7cvt_f16PKfS0_PDF16_S1_iPj:
	s_load_dwordx8 s[8:15], s[0:1], 0x0
	s_cmp_eq_u32 s2, 0
	s_cbranch_scc0 .Lcvt_nozero
	s_load_dwordx2 s[18:19], s[0:1], 0x28
	v_lshlrev_b32_e32 v1, 2, v0
	v_mov_b32_e32 v2, 0
	s_waitcnt lgkmcnt(0)
	global_store_dword v1, v2, s[18:19]
	global_store_dword v1, v2, s[18:19] offset:1024
	global_store_dword v1, v2, s[18:19] offset:2048
.Lcvt_nozero:
	s_waitcnt lgkmcnt(0)
	s_cmp_lt_u32 s2, 0x180
	s_cselect_b32 s3, 0, 0x180
	s_cselect_b32 s4, s8, s10
	s_cselect_b32 s5, s9, s11
	s_cselect_b32 s6, s12, s14
	s_cselect_b32 s7, s13, s15
	s_sub_i32 s3, s2, s3
	v_readfirstlane_b32 s16, v0
	v_and_b32_e32 v1, 63, v0
	s_lshr_b32 s16, s16, 6
	s_lshl_b32 s17, s3, 2
	s_add_i32 s17, s17, s16
	s_lshl_b32 s20, s17, 13
	s_lshl_b32 s21, s17, 12
	s_add_u32 s4, s4, s20
	s_addc_u32 s5, s5, 0
	s_add_u32 s6, s6, s21
	s_addc_u32 s7, s7, 0
	v_lshlrev_b32_e32 v2, 4, v1
	v_add_u32_e32 v3, 0x1000, v2
	global_load_dwordx4 v[8:11], v2, s[4:5] nt
	global_load_dwordx4 v[12:15], v2, s[4:5] offset:1024 nt
	global_load_dwordx4 v[16:19], v2, s[4:5] offset:2048 nt
	global_load_dwordx4 v[20:23], v2, s[4:5] offset:3072 nt
	global_load_dwordx4 v[24:27], v3, s[4:5] nt
	global_load_dwordx4 v[28:31], v3, s[4:5] offset:1024 nt
	global_load_dwordx4 v[32:35], v3, s[4:5] offset:2048 nt
	global_load_dwordx4 v[36:39], v3, s[4:5] offset:3072 nt
	v_and_b32_e32 v4, 1, v1
	v_lshrrev_b32_e32 v5, 1, v1
	v_lshlrev_b32_e32 v6, 9, v4
	v_lshl_add_u32 v6, v5, 4, v6
	v_cmp_eq_u32_e64 s[22:23], 0, v4
	s_waitcnt vmcnt(6)
	v_cvt_pk_f16_f32 v40, v8, v9
	v_cvt_pk_f16_f32 v41, v10, v11
	v_cvt_pk_f16_f32 v42, v12, v13
	v_cvt_pk_f16_f32 v43, v14, v15
	v_cndmask_b32_e64 v44, v40, v42, s[22:23]
	v_cndmask_b32_e64 v45, v41, v43, s[22:23]
	s_nop 0
	v_mov_b32_dpp v46, v44 quad_perm:[1,0,3,2] row_mask:0xf bank_mask:0xf
	v_mov_b32_dpp v47, v45 quad_perm:[1,0,3,2] row_mask:0xf bank_mask:0xf
	v_cndmask_b32_e64 v48, v46, v40, s[22:23]
	v_cndmask_b32_e64 v49, v47, v41, s[22:23]
	v_cndmask_b32_e64 v50, v42, v46, s[22:23]
	v_cndmask_b32_e64 v51, v43, v47, s[22:23]
	global_store_dwordx4 v6, v[48:51], s[6:7] sc1
	s_waitcnt vmcnt(5)
	v_cvt_pk_f16_f32 v40, v16, v17
	v_cvt_pk_f16_f32 v41, v18, v19
	v_cvt_pk_f16_f32 v42, v20, v21
	v_cvt_pk_f16_f32 v43, v22, v23
	v_cndmask_b32_e64 v44, v40, v42, s[22:23]
	v_cndmask_b32_e64 v45, v41, v43, s[22:23]
	s_nop 0
	v_mov_b32_dpp v46, v44 quad_perm:[1,0,3,2] row_mask:0xf bank_mask:0xf
	v_mov_b32_dpp v47, v45 quad_perm:[1,0,3,2] row_mask:0xf bank_mask:0xf
	v_cndmask_b32_e64 v52, v46, v40, s[22:23]
	v_cndmask_b32_e64 v53, v47, v41, s[22:23]
	v_cndmask_b32_e64 v54, v42, v46, s[22:23]
	v_cndmask_b32_e64 v55, v43, v47, s[22:23]
	global_store_dwordx4 v6, v[52:55], s[6:7] offset:1024 sc1
	s_waitcnt vmcnt(4)
	v_cvt_pk_f16_f32 v40, v24, v25
	v_cvt_pk_f16_f32 v41, v26, v27
	v_cvt_pk_f16_f32 v42, v28, v29
	v_cvt_pk_f16_f32 v43, v30, v31
	v_cndmask_b32_e64 v44, v40, v42, s[22:23]
	v_cndmask_b32_e64 v45, v41, v43, s[22:23]
	s_nop 0
	v_mov_b32_dpp v46, v44 quad_perm:[1,0,3,2] row_mask:0xf bank_mask:0xf
	v_mov_b32_dpp v47, v45 quad_perm:[1,0,3,2] row_mask:0xf bank_mask:0xf
	v_cndmask_b32_e64 v56, v46, v40, s[22:23]
	v_cndmask_b32_e64 v57, v47, v41, s[22:23]
	v_cndmask_b32_e64 v58, v42, v46, s[22:23]
	v_cndmask_b32_e64 v59, v43, v47, s[22:23]
	global_store_dwordx4 v6, v[56:59], s[6:7] offset:2048 sc1
	s_waitcnt vmcnt(3)
	v_cvt_pk_f16_f32 v40, v32, v33
	v_cvt_pk_f16_f32 v41, v34, v35
	v_cvt_pk_f16_f32 v42, v36, v37
	v_cvt_pk_f16_f32 v43, v38, v39
	v_cndmask_b32_e64 v44, v40, v42, s[22:23]
	v_cndmask_b32_e64 v45, v41, v43, s[22:23]
	s_nop 0
	v_mov_b32_dpp v46, v44 quad_perm:[1,0,3,2] row_mask:0xf bank_mask:0xf
	v_mov_b32_dpp v47, v45 quad_perm:[1,0,3,2] row_mask:0xf bank_mask:0xf
	v_cndmask_b32_e64 v60, v46, v40, s[22:23]
	v_cndmask_b32_e64 v61, v47, v41, s[22:23]
	v_cndmask_b32_e64 v62, v42, v46, s[22:23]
	v_cndmask_b32_e64 v63, v43, v47, s[22:23]
	global_store_dwordx4 v6, v[60:63], s[6:7] offset:3072 sc1
	s_endpgm

	.amdhsa_kernel _Z7cvt_f16PKfS0_PDF16_S1_iPj
		.amdhsa_group_segment_fixed_size 0
		.amdhsa_private_segment_fixed_size 0
		.amdhsa_kernarg_size 48
		.amdhsa_user_sgpr_count 2
		.amdhsa_user_sgpr_dispatch_ptr 0
		.amdhsa_user_sgpr_queue_ptr 0
		.amdhsa_user_sgpr_kernarg_segment_ptr 1
		.amdhsa_user_sgpr_dispatch_id 0
		.amdhsa_user_sgpr_kernarg_preload_length 0
		.amdhsa_user_sgpr_kernarg_preload_offset 0
		.amdhsa_user_sgpr_private_segment_size 0
		.amdhsa_uses_dynamic_stack 0
		.amdhsa_enable_private_segment 0
		.amdhsa_system_sgpr_workgroup_id_x 1
		.amdhsa_system_sgpr_workgroup_id_y 0
		.amdhsa_system_sgpr_workgroup_id_z 0
		.amdhsa_system_sgpr_workgroup_info 0
		.amdhsa_system_vgpr_workitem_id 0
		.amdhsa_next_free_vgpr 64
		.amdhsa_next_free_sgpr 26
		.amdhsa_accum_offset 64
		.amdhsa_reserve_vcc 1
		.amdhsa_float_round_mode_32 0
		.amdhsa_float_round_mode_16_64 0
		.amdhsa_float_denorm_mode_32 3
		.amdhsa_float_denorm_mode_16_64 3
		.amdhsa_dx10_clamp 1
		.amdhsa_ieee_mode 1
		.amdhsa_fp16_overflow 0
		.amdhsa_tg_split 0
		.amdhsa_exception_fp_ieee_invalid_op 0
		.amdhsa_exception_fp_denorm_src 0
		.amdhsa_exception_fp_ieee_div_zero 0
		.amdhsa_exception_fp_ieee_overflow 0
		.amdhsa_exception_fp_ieee_underflow 0
		.amdhsa_exception_fp_ieee_inexact 0
		.amdhsa_exception_int_div_zero 0
	.end_amdhsa_kernel

amdhsa.kernels:
  - .agpr_count:     0
    .args:
      - .actual_access:  read_only
        .address_space:  global
        .offset:         0
        .size:           8
        .value_kind:     global_buffer
      - .actual_access:  read_only
        .address_space:  global
        .offset:         8
        .size:           8
        .value_kind:     global_buffer
      - .address_space:  global
        .offset:         16
        .size:           8
        .value_kind:     global_buffer
      - .address_space:  global
        .offset:         24
        .size:           8
        .value_kind:     global_buffer
      - .offset:         32
        .size:           4
        .value_kind:     by_value
      - .actual_access:  write_only
        .address_space:  global
        .offset:         40
        .size:           8
        .value_kind:     global_buffer
    .group_segment_fixed_size: 0
    .kernarg_segment_align: 8
    .kernarg_segment_size: 48
    .language:       OpenCL C
    .language_version:
      - 2
      - 0
    .max_flat_workgroup_size: 256
    .name:           _Z7cvt_f16PKfS0_PDF16_S1_iPj
    .private_segment_fixed_size: 0
    .sgpr_count:     32
    .sgpr_spill_count: 0
    .symbol:         _Z7cvt_f16PKfS0_PDF16_S1_iPj.kd
    .uniform_work_group_size: 1
    .uses_dynamic_stack: false
    .vgpr_count:     64
    .vgpr_spill_count: 0
    .wavefront_size: 64
  - .agpr_count:     0
    .args:
      - .address_space:  global
        .offset:         0
        .size:           8
        .value_kind:     global_buffer
      - .address_space:  global
        .offset:         8
        .size:           8
        .value_kind:     global_buffer
      - .actual_access:  read_only
        .address_space:  global
        .offset:         16
        .size:           8
        .value_kind:     global_buffer
      - .address_space:  global
        .offset:         24
        .size:           8
        .value_kind:     global_buffer
      - .address_space:  global
        .offset:         32
        .size:           8
        .value_kind:     global_buffer
      - .address_space:  global
        .offset:         40
        .size:           8
        .value_kind:     global_buffer
      - .address_space:  global
        .offset:         48
        .size:           8
        .value_kind:     global_buffer
    .group_segment_fixed_size: 1024
    .kernarg_segment_align: 8
    .kernarg_segment_size: 56
    .language:       OpenCL C
    .language_version:
      - 2
      - 0
    .max_flat_workgroup_size: 512
    .name:           _Z8gemm_qkvPKDF16_S0_PKfPDF16_S3_S3_Pj
    .private_segment_fixed_size: 0
    .sgpr_count:     62
    .sgpr_spill_count: 0
    .symbol:         _Z8gemm_qkvPKDF16_S0_PKfPDF16_S3_S3_Pj.kd
    .uniform_work_group_size: 1
    .uses_dynamic_stack: false
    .vgpr_count:     256
    .vgpr_spill_count: 0
    .wavefront_size: 64
  - .agpr_count:     0
    .args:
      - .actual_access:  read_only
        .address_space:  global
        .offset:         0
        .size:           8
        .value_kind:     global_buffer
      - .address_space:  global
        .offset:         8
        .size:           8
        .value_kind:     global_buffer
      - .address_space:  global
        .offset:         16
        .size:           8
        .value_kind:     global_buffer
      - .actual_access:  read_only
        .address_space:  global
        .offset:         24
        .size:           8
        .value_kind:     global_buffer
      - .address_space:  global
        .offset:         32
        .size:           8
        .value_kind:     global_buffer
    .group_segment_fixed_size: 132896
    .kernarg_segment_align: 8
    .kernarg_segment_size: 40
    .language:       OpenCL C
    .language_version:
      - 2
      - 0
    .max_flat_workgroup_size: 512
    .name:           _Z8attn_fwdPKDF16_S0_S0_PKjPf
    .private_segment_fixed_size: 0
    .sgpr_count:     41
    .sgpr_spill_count: 0
    .symbol:         _Z8attn_fwdPKDF16_S0_S0_PKjPf.kd
    .uniform_work_group_size: 1
    .uses_dynamic_stack: false
    .vgpr_count:     242
    .vgpr_spill_count: 0
    .wavefront_size: 64
